# P0 weight transposes (ev_w_in, peer_wq L0): 16 row loads + 16 gain loads of a tile in flight together instead of one round trip per element
# speedup vs baseline: 1.0050x; 1.0050x over previous
; #define LAS __attribute__((address_space(3)))
; #define LDS_WAIT() asm volatile("s_waitcnt lgkmcnt(0)" ::: "memory")
; __device__ __forceinline__ void p0_transpose_item(const float* W, int K, int N, bf16_t* WT, const float* g, bool remap, LAS float* scr, int item, int lane) {
;     const int nblk = (N + 31) / 32, kb = item / nblk, nb = item % nblk, k0 = 64 * kb, n0 = 32 * nb;
; #pragma unroll 8
;     for (int i = 0; i < 32; ++i) { const int kk = 2 * i + (lane >> 5), n = n0 + (lane & 31);
;         float v = (n < N) ? W[(size_t)(k0 + kk) * N + n] : 0.f; if (g) v *= g[k0 + kk]; scr[kk * 33 + (lane & 31)] = v; }
;     LDS_WAIT(); asm volatile("" ::: "memory");
.LBB0_75:
	s_and_b64 vcc, exec, s[26:27]
	s_cbranch_vccz .Lp0t3_slow
	v_mov_b64_e32 v[140:141], v[64:65]
	s_mov_b64 s[0:1], 0x4000
	v_lshl_add_u64 v[176:177], s[14:15], 0, v[62:63]
	global_load_dword v144, v[140:141], off
	v_lshl_add_u64 v[142:143], v[140:141], 0, s[0:1]
	global_load_dword v145, v[142:143], off
	v_lshl_add_u64 v[140:141], v[142:143], 0, s[0:1]
	global_load_dword v146, v[140:141], off
	v_lshl_add_u64 v[142:143], v[140:141], 0, s[0:1]
	global_load_dword v147, v[142:143], off
	v_lshl_add_u64 v[140:141], v[142:143], 0, s[0:1]
	global_load_dword v148, v[140:141], off
	v_lshl_add_u64 v[142:143], v[140:141], 0, s[0:1]
	global_load_dword v149, v[142:143], off
	v_lshl_add_u64 v[140:141], v[142:143], 0, s[0:1]
	global_load_dword v150, v[140:141], off
	v_lshl_add_u64 v[142:143], v[140:141], 0, s[0:1]
	global_load_dword v151, v[142:143], off
	v_lshl_add_u64 v[140:141], v[142:143], 0, s[0:1]
	global_load_dword v152, v[140:141], off
	v_lshl_add_u64 v[142:143], v[140:141], 0, s[0:1]
	global_load_dword v153, v[142:143], off
	v_lshl_add_u64 v[140:141], v[142:143], 0, s[0:1]
	global_load_dword v154, v[140:141], off
	v_lshl_add_u64 v[142:143], v[140:141], 0, s[0:1]
	global_load_dword v155, v[142:143], off
	v_lshl_add_u64 v[140:141], v[142:143], 0, s[0:1]
	global_load_dword v156, v[140:141], off
	v_lshl_add_u64 v[142:143], v[140:141], 0, s[0:1]
	global_load_dword v157, v[142:143], off
	v_lshl_add_u64 v[140:141], v[142:143], 0, s[0:1]
	global_load_dword v158, v[140:141], off
	v_lshl_add_u64 v[142:143], v[140:141], 0, s[0:1]
	global_load_dword v159, v[142:143], off
	v_lshl_add_u64 v[140:141], v[142:143], 0, s[0:1]
	global_load_dword v160, v[176:177], off
	global_load_dword v161, v[176:177], off offset:8
	global_load_dword v162, v[176:177], off offset:16
	global_load_dword v163, v[176:177], off offset:24
	global_load_dword v164, v[176:177], off offset:32
	global_load_dword v165, v[176:177], off offset:40
	global_load_dword v166, v[176:177], off offset:48
	global_load_dword v167, v[176:177], off offset:56
	global_load_dword v168, v[176:177], off offset:64
	global_load_dword v169, v[176:177], off offset:72
	global_load_dword v170, v[176:177], off offset:80
	global_load_dword v171, v[176:177], off offset:88
	global_load_dword v172, v[176:177], off offset:96
	global_load_dword v173, v[176:177], off offset:104
	global_load_dword v174, v[176:177], off offset:112
	global_load_dword v175, v[176:177], off offset:120
	s_waitcnt vmcnt(0)
	v_mul_f32_e32 v144, v144, v160
	ds_write_b32 v43, v144
	v_mul_f32_e32 v145, v145, v161
	ds_write_b32 v43, v145 offset:264
	v_mul_f32_e32 v146, v146, v162
	ds_write_b32 v43, v146 offset:528
	v_mul_f32_e32 v147, v147, v163
	ds_write_b32 v43, v147 offset:792
	v_mul_f32_e32 v148, v148, v164
	ds_write_b32 v43, v148 offset:1056
	v_mul_f32_e32 v149, v149, v165
	ds_write_b32 v43, v149 offset:1320
	v_mul_f32_e32 v150, v150, v166
	ds_write_b32 v43, v150 offset:1584
	v_mul_f32_e32 v151, v151, v167
	ds_write_b32 v43, v151 offset:1848
	v_mul_f32_e32 v152, v152, v168
	ds_write_b32 v43, v152 offset:2112
	v_mul_f32_e32 v153, v153, v169
	ds_write_b32 v43, v153 offset:2376
	v_mul_f32_e32 v154, v154, v170
	ds_write_b32 v43, v154 offset:2640
	v_mul_f32_e32 v155, v155, v171
	ds_write_b32 v43, v155 offset:2904
	v_mul_f32_e32 v156, v156, v172
	ds_write_b32 v43, v156 offset:3168
	v_mul_f32_e32 v157, v157, v173
	ds_write_b32 v43, v157 offset:3432
	v_mul_f32_e32 v158, v158, v174
	ds_write_b32 v43, v158 offset:3696
	v_mul_f32_e32 v159, v159, v175
	ds_write_b32 v43, v159 offset:3960
	global_load_dword v144, v[140:141], off
	v_lshl_add_u64 v[142:143], v[140:141], 0, s[0:1]
	global_load_dword v145, v[142:143], off
	v_lshl_add_u64 v[140:141], v[142:143], 0, s[0:1]
	global_load_dword v146, v[140:141], off
	v_lshl_add_u64 v[142:143], v[140:141], 0, s[0:1]
	global_load_dword v147, v[142:143], off
	v_lshl_add_u64 v[140:141], v[142:143], 0, s[0:1]
	global_load_dword v148, v[140:141], off
	v_lshl_add_u64 v[142:143], v[140:141], 0, s[0:1]
	global_load_dword v149, v[142:143], off
	v_lshl_add_u64 v[140:141], v[142:143], 0, s[0:1]
	global_load_dword v150, v[140:141], off
	v_lshl_add_u64 v[142:143], v[140:141], 0, s[0:1]
	global_load_dword v151, v[142:143], off
	v_lshl_add_u64 v[140:141], v[142:143], 0, s[0:1]
	global_load_dword v152, v[140:141], off
	v_lshl_add_u64 v[142:143], v[140:141], 0, s[0:1]
	global_load_dword v153, v[142:143], off
	v_lshl_add_u64 v[140:141], v[142:143], 0, s[0:1]
	global_load_dword v154, v[140:141], off
	v_lshl_add_u64 v[142:143], v[140:141], 0, s[0:1]
	global_load_dword v155, v[142:143], off
	v_lshl_add_u64 v[140:141], v[142:143], 0, s[0:1]
	global_load_dword v156, v[140:141], off
	v_lshl_add_u64 v[142:143], v[140:141], 0, s[0:1]
	global_load_dword v157, v[142:143], off
	v_lshl_add_u64 v[140:141], v[142:143], 0, s[0:1]
	global_load_dword v158, v[140:141], off
	v_lshl_add_u64 v[142:143], v[140:141], 0, s[0:1]
	global_load_dword v159, v[142:143], off
	global_load_dword v160, v[176:177], off offset:128
	global_load_dword v161, v[176:177], off offset:136
	global_load_dword v162, v[176:177], off offset:144
	global_load_dword v163, v[176:177], off offset:152
	global_load_dword v164, v[176:177], off offset:160
	global_load_dword v165, v[176:177], off offset:168
	global_load_dword v166, v[176:177], off offset:176
	global_load_dword v167, v[176:177], off offset:184
	global_load_dword v168, v[176:177], off offset:192
	global_load_dword v169, v[176:177], off offset:200
	global_load_dword v170, v[176:177], off offset:208
	global_load_dword v171, v[176:177], off offset:216
	global_load_dword v172, v[176:177], off offset:224
	global_load_dword v173, v[176:177], off offset:232
	global_load_dword v174, v[176:177], off offset:240
	global_load_dword v175, v[176:177], off offset:248
	s_waitcnt vmcnt(0)
	v_mul_f32_e32 v144, v144, v160
	ds_write_b32 v43, v144 offset:4224
	v_mul_f32_e32 v145, v145, v161
	ds_write_b32 v43, v145 offset:4488
	v_mul_f32_e32 v146, v146, v162
	ds_write_b32 v43, v146 offset:4752
	v_mul_f32_e32 v147, v147, v163
	ds_write_b32 v43, v147 offset:5016
	v_mul_f32_e32 v148, v148, v164
	ds_write_b32 v43, v148 offset:5280
	v_mul_f32_e32 v149, v149, v165
	ds_write_b32 v43, v149 offset:5544
	v_mul_f32_e32 v150, v150, v166
	ds_write_b32 v43, v150 offset:5808
	v_mul_f32_e32 v151, v151, v167
	ds_write_b32 v43, v151 offset:6072
	v_mul_f32_e32 v152, v152, v168
	ds_write_b32 v43, v152 offset:6336
	v_mul_f32_e32 v153, v153, v169
	ds_write_b32 v43, v153 offset:6600
	v_mul_f32_e32 v154, v154, v170
	ds_write_b32 v43, v154 offset:6864
	v_mul_f32_e32 v155, v155, v171
	ds_write_b32 v43, v155 offset:7128
	v_mul_f32_e32 v156, v156, v172
	ds_write_b32 v43, v156 offset:7392
	v_mul_f32_e32 v157, v157, v173
	ds_write_b32 v43, v157 offset:7656
	v_mul_f32_e32 v158, v158, v174
	ds_write_b32 v43, v158 offset:7920
	v_mul_f32_e32 v159, v159, v175
	ds_write_b32 v43, v159 offset:8184
	s_branch .LBB0_91

; __device__ __forceinline__ void p0_transpose_item(const float* W, int K, int N, bf16_t* WT, const float* g, bool remap, LAS float* scr, int item, int lane) {
;     ...
; #pragma unroll 8
;     for (int i = 0; i < 32; ++i) { const int kk = 2 * i + (lane >> 5), n = n0 + (lane & 31);
;         float v = (n < N) ? W[(size_t)(k0 + kk) * N + n] : 0.f; if (g) v *= g[k0 + kk]; scr[kk * 33 + (lane & 31)] = v; }
.LBB0_143:
	s_and_b64 vcc, exec, s[30:31]
	s_cbranch_vccz .Lp0t7_slow
	v_readlane_b32 s58, v237, 13
	v_readlane_b32 s59, v237, 14
	v_mad_i64_i32 v[140:141], s[36:37], v43, s51, v[46:47]
	s_lshl_b32 s14, s51, 1
	s_mov_b32 s15, 0
	v_ashrrev_i32_e32 v177, 31, v43
	v_mov_b32_e32 v176, v43
	s_nop 0
	v_lshl_add_u64 v[176:177], v[176:177], 2, s[58:59]
	v_mov_b32_e32 v144, 0
	v_mov_b32_e32 v145, 0
	v_mov_b32_e32 v146, 0
	v_mov_b32_e32 v147, 0
	v_mov_b32_e32 v148, 0
	v_mov_b32_e32 v149, 0
	v_mov_b32_e32 v150, 0
	v_mov_b32_e32 v151, 0
	v_mov_b32_e32 v152, 0
	v_mov_b32_e32 v153, 0
	v_mov_b32_e32 v154, 0
	v_mov_b32_e32 v155, 0
	v_mov_b32_e32 v156, 0
	v_mov_b32_e32 v157, 0
	v_mov_b32_e32 v158, 0
	v_mov_b32_e32 v159, 0
	s_and_saveexec_b64 s[36:37], s[12:13]
	s_cbranch_execz .Lp0t7_nl0
	global_load_dword v144, v[140:141], off
	v_lshl_add_u64 v[142:143], v[140:141], 0, s[14:15]
	global_load_dword v145, v[142:143], off
	v_lshl_add_u64 v[140:141], v[142:143], 0, s[14:15]
	global_load_dword v146, v[140:141], off
	v_lshl_add_u64 v[142:143], v[140:141], 0, s[14:15]
	global_load_dword v147, v[142:143], off
	v_lshl_add_u64 v[140:141], v[142:143], 0, s[14:15]
	global_load_dword v148, v[140:141], off
	v_lshl_add_u64 v[142:143], v[140:141], 0, s[14:15]
	global_load_dword v149, v[142:143], off
	v_lshl_add_u64 v[140:141], v[142:143], 0, s[14:15]
	global_load_dword v150, v[140:141], off
	v_lshl_add_u64 v[142:143], v[140:141], 0, s[14:15]
	global_load_dword v151, v[142:143], off
	v_lshl_add_u64 v[140:141], v[142:143], 0, s[14:15]
	global_load_dword v152, v[140:141], off
	v_lshl_add_u64 v[142:143], v[140:141], 0, s[14:15]
	global_load_dword v153, v[142:143], off
	v_lshl_add_u64 v[140:141], v[142:143], 0, s[14:15]
	global_load_dword v154, v[140:141], off
	v_lshl_add_u64 v[142:143], v[140:141], 0, s[14:15]
	global_load_dword v155, v[142:143], off
	v_lshl_add_u64 v[140:141], v[142:143], 0, s[14:15]
	global_load_dword v156, v[140:141], off
	v_lshl_add_u64 v[142:143], v[140:141], 0, s[14:15]
	global_load_dword v157, v[142:143], off
	v_lshl_add_u64 v[140:141], v[142:143], 0, s[14:15]
	global_load_dword v158, v[140:141], off
	v_lshl_add_u64 v[142:143], v[140:141], 0, s[14:15]
	global_load_dword v159, v[142:143], off
	v_lshl_add_u64 v[140:141], v[142:143], 0, s[14:15]
; #define LDS_WAIT() asm volatile("s_waitcnt lgkmcnt(0)" ::: "memory")
; __device__ __forceinline__ void p0_transpose_item(const float* W, int K, int N, bf16_t* WT, const float* g, bool remap, LAS float* scr, int item, int lane) {
;     ...
; #pragma unroll 8
;     for (int i = 0; i < 32; ++i) { const int kk = 2 * i + (lane >> 5), n = n0 + (lane & 31);
;         float v = (n < N) ? W[(size_t)(k0 + kk) * N + n] : 0.f; if (g) v *= g[k0 + kk]; scr[kk * 33 + (lane & 31)] = v; }
;     LDS_WAIT(); asm volatile("" ::: "memory");
.Lp0t7_nl0:
	s_or_b64 exec, exec, s[36:37]
	global_load_dword v160, v[176:177], off
	global_load_dword v161, v[176:177], off offset:8
	global_load_dword v162, v[176:177], off offset:16
	global_load_dword v163, v[176:177], off offset:24
	global_load_dword v164, v[176:177], off offset:32
	global_load_dword v165, v[176:177], off offset:40
	global_load_dword v166, v[176:177], off offset:48
	global_load_dword v167, v[176:177], off offset:56
	global_load_dword v168, v[176:177], off offset:64
	global_load_dword v169, v[176:177], off offset:72
	global_load_dword v170, v[176:177], off offset:80
	global_load_dword v171, v[176:177], off offset:88
	global_load_dword v172, v[176:177], off offset:96
	global_load_dword v173, v[176:177], off offset:104
	global_load_dword v174, v[176:177], off offset:112
	global_load_dword v175, v[176:177], off offset:120
	s_waitcnt vmcnt(0)
	v_mul_f32_e32 v144, v144, v160
	ds_write_b32 v52, v144
	v_mul_f32_e32 v145, v145, v161
	ds_write_b32 v52, v145 offset:264
	v_mul_f32_e32 v146, v146, v162
	ds_write_b32 v52, v146 offset:528
	v_mul_f32_e32 v147, v147, v163
	ds_write_b32 v52, v147 offset:792
	v_mul_f32_e32 v148, v148, v164
	ds_write_b32 v52, v148 offset:1056
	v_mul_f32_e32 v149, v149, v165
	ds_write_b32 v52, v149 offset:1320
	v_mul_f32_e32 v150, v150, v166
	ds_write_b32 v52, v150 offset:1584
	v_mul_f32_e32 v151, v151, v167
	ds_write_b32 v52, v151 offset:1848
	v_mul_f32_e32 v152, v152, v168
	ds_write_b32 v52, v152 offset:2112
	v_mul_f32_e32 v153, v153, v169
	ds_write_b32 v52, v153 offset:2376
	v_mul_f32_e32 v154, v154, v170
	ds_write_b32 v52, v154 offset:2640
	v_mul_f32_e32 v155, v155, v171
	ds_write_b32 v52, v155 offset:2904
	v_mul_f32_e32 v156, v156, v172
	ds_write_b32 v52, v156 offset:3168
	v_mul_f32_e32 v157, v157, v173
	ds_write_b32 v52, v157 offset:3432
	v_mul_f32_e32 v158, v158, v174
	ds_write_b32 v52, v158 offset:3696
	v_mul_f32_e32 v159, v159, v175
	ds_write_b32 v52, v159 offset:3960
	v_mov_b32_e32 v144, 0
	v_mov_b32_e32 v145, 0
	v_mov_b32_e32 v146, 0
	v_mov_b32_e32 v147, 0
	v_mov_b32_e32 v148, 0
	v_mov_b32_e32 v149, 0
	v_mov_b32_e32 v150, 0
	v_mov_b32_e32 v151, 0
	v_mov_b32_e32 v152, 0
	v_mov_b32_e32 v153, 0
	v_mov_b32_e32 v154, 0
	v_mov_b32_e32 v155, 0
	v_mov_b32_e32 v156, 0
	v_mov_b32_e32 v157, 0
	v_mov_b32_e32 v158, 0
	v_mov_b32_e32 v159, 0
	s_and_saveexec_b64 s[36:37], s[12:13]
	s_cbranch_execz .Lp0t7_nl1
	global_load_dword v144, v[140:141], off
	v_lshl_add_u64 v[142:143], v[140:141], 0, s[14:15]
	global_load_dword v145, v[142:143], off
	v_lshl_add_u64 v[140:141], v[142:143], 0, s[14:15]
	global_load_dword v146, v[140:141], off
	v_lshl_add_u64 v[142:143], v[140:141], 0, s[14:15]
	global_load_dword v147, v[142:143], off
	v_lshl_add_u64 v[140:141], v[142:143], 0, s[14:15]
	global_load_dword v148, v[140:141], off
	v_lshl_add_u64 v[142:143], v[140:141], 0, s[14:15]
	global_load_dword v149, v[142:143], off
	v_lshl_add_u64 v[140:141], v[142:143], 0, s[14:15]
	global_load_dword v150, v[140:141], off
	v_lshl_add_u64 v[142:143], v[140:141], 0, s[14:15]
	global_load_dword v151, v[142:143], off
	v_lshl_add_u64 v[140:141], v[142:143], 0, s[14:15]
	global_load_dword v152, v[140:141], off
	v_lshl_add_u64 v[142:143], v[140:141], 0, s[14:15]
	global_load_dword v153, v[142:143], off
	v_lshl_add_u64 v[140:141], v[142:143], 0, s[14:15]
	global_load_dword v154, v[140:141], off
	v_lshl_add_u64 v[142:143], v[140:141], 0, s[14:15]
	global_load_dword v155, v[142:143], off
	v_lshl_add_u64 v[140:141], v[142:143], 0, s[14:15]
	global_load_dword v156, v[140:141], off
	v_lshl_add_u64 v[142:143], v[140:141], 0, s[14:15]
	global_load_dword v157, v[142:143], off
	v_lshl_add_u64 v[140:141], v[142:143], 0, s[14:15]
	global_load_dword v158, v[140:141], off
	v_lshl_add_u64 v[142:143], v[140:141], 0, s[14:15]
	global_load_dword v159, v[142:143], off
.Lp0t7_nl1:
	s_or_b64 exec, exec, s[36:37]
	global_load_dword v160, v[176:177], off offset:128
	global_load_dword v161, v[176:177], off offset:136
	global_load_dword v162, v[176:177], off offset:144
	global_load_dword v163, v[176:177], off offset:152
	global_load_dword v164, v[176:177], off offset:160
	global_load_dword v165, v[176:177], off offset:168
	global_load_dword v166, v[176:177], off offset:176
	global_load_dword v167, v[176:177], off offset:184
	global_load_dword v168, v[176:177], off offset:192
	global_load_dword v169, v[176:177], off offset:200
	global_load_dword v170, v[176:177], off offset:208
	global_load_dword v171, v[176:177], off offset:216
	global_load_dword v172, v[176:177], off offset:224
	global_load_dword v173, v[176:177], off offset:232
	global_load_dword v174, v[176:177], off offset:240
	global_load_dword v175, v[176:177], off offset:248
	s_waitcnt vmcnt(0)
	v_mul_f32_e32 v144, v144, v160
	ds_write_b32 v52, v144 offset:4224
	v_mul_f32_e32 v145, v145, v161
	ds_write_b32 v52, v145 offset:4488
	v_mul_f32_e32 v146, v146, v162
	ds_write_b32 v52, v146 offset:4752
	v_mul_f32_e32 v147, v147, v163
	ds_write_b32 v52, v147 offset:5016
	v_mul_f32_e32 v148, v148, v164
	ds_write_b32 v52, v148 offset:5280
	v_mul_f32_e32 v149, v149, v165
	ds_write_b32 v52, v149 offset:5544
	v_mul_f32_e32 v150, v150, v166
	ds_write_b32 v52, v150 offset:5808
	v_mul_f32_e32 v151, v151, v167
	ds_write_b32 v52, v151 offset:6072
	v_mul_f32_e32 v152, v152, v168
	ds_write_b32 v52, v152 offset:6336
	v_mul_f32_e32 v153, v153, v169
	ds_write_b32 v52, v153 offset:6600
	v_mul_f32_e32 v154, v154, v170
	ds_write_b32 v52, v154 offset:6864
	v_mul_f32_e32 v155, v155, v171
	ds_write_b32 v52, v155 offset:7128
	v_mul_f32_e32 v156, v156, v172
	ds_write_b32 v52, v156 offset:7392
	v_mul_f32_e32 v157, v157, v173
	ds_write_b32 v52, v157 offset:7656
	v_mul_f32_e32 v158, v158, v174
	ds_write_b32 v52, v158 offset:7920
	v_mul_f32_e32 v159, v159, v175
	ds_write_b32 v52, v159 offset:8184
	s_branch .LBB0_175
